# phase 1 light jobs: FoX-norm loads batched together, MoBA block-mean 64 loads in flight
# baseline (speedup 1.0000x reference)
.LBB0_351:
	v_add_co_u32_e32 v0, vcc, 0xffff9800, v0
	s_nop 1
	v_addc_co_u32_e32 v1, vcc, -1, v1, vcc
	s_mov_b64 s[30:31], 0x2000
	global_load_dwordx2 v[112:113], v[0:1], off offset:-4096
	global_load_dwordx2 v[114:115], v[0:1], off offset:-2048
	global_load_dwordx2 v[116:117], v[0:1], off
	global_load_dwordx2 v[118:119], v[0:1], off offset:2048
	v_lshl_add_u64 v[0:1], v[0:1], 0, s[30:31]
	global_load_dwordx2 v[120:121], v[0:1], off offset:-4096
	global_load_dwordx2 v[122:123], v[0:1], off offset:-2048
	global_load_dwordx2 v[124:125], v[0:1], off
	global_load_dwordx2 v[126:127], v[0:1], off offset:2048
	v_lshl_add_u64 v[0:1], v[0:1], 0, s[30:31]
	global_load_dwordx2 v[128:129], v[0:1], off offset:-4096
	global_load_dwordx2 v[130:131], v[0:1], off offset:-2048
	global_load_dwordx2 v[132:133], v[0:1], off
	global_load_dwordx2 v[134:135], v[0:1], off offset:2048
	v_lshl_add_u64 v[0:1], v[0:1], 0, s[30:31]
	global_load_dwordx2 v[136:137], v[0:1], off offset:-4096
	global_load_dwordx2 v[138:139], v[0:1], off offset:-2048
	global_load_dwordx2 v[140:141], v[0:1], off
	global_load_dwordx2 v[142:143], v[0:1], off offset:2048
	v_lshl_add_u64 v[0:1], v[0:1], 0, s[30:31]
	global_load_dwordx2 v[144:145], v[0:1], off offset:-4096
	global_load_dwordx2 v[146:147], v[0:1], off offset:-2048
	global_load_dwordx2 v[148:149], v[0:1], off
	global_load_dwordx2 v[150:151], v[0:1], off offset:2048
	v_lshl_add_u64 v[0:1], v[0:1], 0, s[30:31]
	global_load_dwordx2 v[152:153], v[0:1], off offset:-4096
	global_load_dwordx2 v[154:155], v[0:1], off offset:-2048
	global_load_dwordx2 v[156:157], v[0:1], off
	global_load_dwordx2 v[158:159], v[0:1], off offset:2048
	v_lshl_add_u64 v[0:1], v[0:1], 0, s[30:31]
	global_load_dwordx2 v[160:161], v[0:1], off offset:-4096
	global_load_dwordx2 v[162:163], v[0:1], off offset:-2048
	global_load_dwordx2 v[164:165], v[0:1], off
	global_load_dwordx2 v[166:167], v[0:1], off offset:2048
	v_lshl_add_u64 v[0:1], v[0:1], 0, s[30:31]
	global_load_dwordx2 v[168:169], v[0:1], off offset:-4096
	global_load_dwordx2 v[170:171], v[0:1], off offset:-2048
	global_load_dwordx2 v[172:173], v[0:1], off
	global_load_dwordx2 v[174:175], v[0:1], off offset:2048
	v_lshl_add_u64 v[0:1], v[0:1], 0, s[30:31]
	global_load_dwordx2 v[176:177], v[0:1], off offset:-4096
	global_load_dwordx2 v[178:179], v[0:1], off offset:-2048
	global_load_dwordx2 v[180:181], v[0:1], off
	global_load_dwordx2 v[182:183], v[0:1], off offset:2048
	v_lshl_add_u64 v[0:1], v[0:1], 0, s[30:31]
	global_load_dwordx2 v[184:185], v[0:1], off offset:-4096
	global_load_dwordx2 v[186:187], v[0:1], off offset:-2048
	global_load_dwordx2 v[188:189], v[0:1], off
	global_load_dwordx2 v[190:191], v[0:1], off offset:2048
	v_lshl_add_u64 v[0:1], v[0:1], 0, s[30:31]
	global_load_dwordx2 v[192:193], v[0:1], off offset:-4096
	global_load_dwordx2 v[194:195], v[0:1], off offset:-2048
	global_load_dwordx2 v[196:197], v[0:1], off
	global_load_dwordx2 v[198:199], v[0:1], off offset:2048
	v_lshl_add_u64 v[0:1], v[0:1], 0, s[30:31]
	global_load_dwordx2 v[200:201], v[0:1], off offset:-4096
	global_load_dwordx2 v[202:203], v[0:1], off offset:-2048
	global_load_dwordx2 v[204:205], v[0:1], off
	global_load_dwordx2 v[206:207], v[0:1], off offset:2048
	v_lshl_add_u64 v[0:1], v[0:1], 0, s[30:31]
	global_load_dwordx2 v[208:209], v[0:1], off offset:-4096
	global_load_dwordx2 v[210:211], v[0:1], off offset:-2048
	global_load_dwordx2 v[212:213], v[0:1], off
	global_load_dwordx2 v[214:215], v[0:1], off offset:2048
	v_lshl_add_u64 v[0:1], v[0:1], 0, s[30:31]
	global_load_dwordx2 v[216:217], v[0:1], off offset:-4096
	global_load_dwordx2 v[218:219], v[0:1], off offset:-2048
	global_load_dwordx2 v[220:221], v[0:1], off
	global_load_dwordx2 v[222:223], v[0:1], off offset:2048
	v_lshl_add_u64 v[0:1], v[0:1], 0, s[30:31]
	global_load_dwordx2 v[6:7], v[0:1], off offset:-4096
	global_load_dwordx2 v[8:9], v[0:1], off offset:-2048
	global_load_dwordx2 v[10:11], v[0:1], off
	global_load_dwordx2 v[12:13], v[0:1], off offset:2048
	v_lshl_add_u64 v[0:1], v[0:1], 0, s[30:31]
	global_load_dwordx2 v[14:15], v[0:1], off offset:-4096
	global_load_dwordx2 v[16:17], v[0:1], off offset:-2048
	global_load_dwordx2 v[18:19], v[0:1], off
	global_load_dwordx2 v[20:21], v[0:1], off offset:2048
	s_waitcnt vmcnt(0)
	v_lshlrev_b32_e32 v82, 16, v112
	v_and_b32_e32 v83, 0xffff0000, v112
	v_pk_add_f32 v[4:5], v[4:5], v[82:83]
	v_lshlrev_b32_e32 v82, 16, v113
	v_and_b32_e32 v83, 0xffff0000, v113
	v_pk_add_f32 v[2:3], v[2:3], v[82:83]
	v_lshlrev_b32_e32 v82, 16, v115
	v_and_b32_e32 v83, 0xffff0000, v115
	v_pk_add_f32 v[2:3], v[2:3], v[82:83]
	v_lshlrev_b32_e32 v82, 16, v114
	v_and_b32_e32 v83, 0xffff0000, v114
	v_pk_add_f32 v[4:5], v[4:5], v[82:83]
	v_lshlrev_b32_e32 v82, 16, v116
	v_and_b32_e32 v83, 0xffff0000, v116
	v_pk_add_f32 v[4:5], v[4:5], v[82:83]
	v_lshlrev_b32_e32 v82, 16, v117
	v_and_b32_e32 v83, 0xffff0000, v117
	v_pk_add_f32 v[2:3], v[2:3], v[82:83]
	v_lshlrev_b32_e32 v82, 16, v119
	v_and_b32_e32 v83, 0xffff0000, v119
	v_pk_add_f32 v[2:3], v[2:3], v[82:83]
	v_lshlrev_b32_e32 v82, 16, v118
	v_and_b32_e32 v83, 0xffff0000, v118
	v_pk_add_f32 v[4:5], v[4:5], v[82:83]
	v_lshlrev_b32_e32 v82, 16, v120
	v_and_b32_e32 v83, 0xffff0000, v120
	v_pk_add_f32 v[4:5], v[4:5], v[82:83]
	v_lshlrev_b32_e32 v82, 16, v121
	v_and_b32_e32 v83, 0xffff0000, v121
	v_pk_add_f32 v[2:3], v[2:3], v[82:83]
	v_lshlrev_b32_e32 v82, 16, v123
	v_and_b32_e32 v83, 0xffff0000, v123
	v_pk_add_f32 v[2:3], v[2:3], v[82:83]
	v_lshlrev_b32_e32 v82, 16, v122
	v_and_b32_e32 v83, 0xffff0000, v122
	v_pk_add_f32 v[4:5], v[4:5], v[82:83]
	v_lshlrev_b32_e32 v82, 16, v124
	v_and_b32_e32 v83, 0xffff0000, v124
	v_pk_add_f32 v[4:5], v[4:5], v[82:83]
	v_lshlrev_b32_e32 v82, 16, v125
	v_and_b32_e32 v83, 0xffff0000, v125
	v_pk_add_f32 v[2:3], v[2:3], v[82:83]
	v_lshlrev_b32_e32 v82, 16, v127
	v_and_b32_e32 v83, 0xffff0000, v127
	v_pk_add_f32 v[2:3], v[2:3], v[82:83]
	v_lshlrev_b32_e32 v82, 16, v126
	v_and_b32_e32 v83, 0xffff0000, v126
	v_pk_add_f32 v[4:5], v[4:5], v[82:83]
	v_lshlrev_b32_e32 v82, 16, v128
	v_and_b32_e32 v83, 0xffff0000, v128
	v_pk_add_f32 v[4:5], v[4:5], v[82:83]
	v_lshlrev_b32_e32 v82, 16, v129
	v_and_b32_e32 v83, 0xffff0000, v129
	v_pk_add_f32 v[2:3], v[2:3], v[82:83]
	v_lshlrev_b32_e32 v82, 16, v131
	v_and_b32_e32 v83, 0xffff0000, v131
	v_pk_add_f32 v[2:3], v[2:3], v[82:83]
	v_lshlrev_b32_e32 v82, 16, v130
	v_and_b32_e32 v83, 0xffff0000, v130
	v_pk_add_f32 v[4:5], v[4:5], v[82:83]
	v_lshlrev_b32_e32 v82, 16, v132
	v_and_b32_e32 v83, 0xffff0000, v132
	v_pk_add_f32 v[4:5], v[4:5], v[82:83]
	v_lshlrev_b32_e32 v82, 16, v133
	v_and_b32_e32 v83, 0xffff0000, v133
	v_pk_add_f32 v[2:3], v[2:3], v[82:83]
	v_lshlrev_b32_e32 v82, 16, v135
	v_and_b32_e32 v83, 0xffff0000, v135
	v_pk_add_f32 v[2:3], v[2:3], v[82:83]
	v_lshlrev_b32_e32 v82, 16, v134
	v_and_b32_e32 v83, 0xffff0000, v134
	v_pk_add_f32 v[4:5], v[4:5], v[82:83]
	v_lshlrev_b32_e32 v82, 16, v136
	v_and_b32_e32 v83, 0xffff0000, v136
	v_pk_add_f32 v[4:5], v[4:5], v[82:83]
	v_lshlrev_b32_e32 v82, 16, v137
	v_and_b32_e32 v83, 0xffff0000, v137
	v_pk_add_f32 v[2:3], v[2:3], v[82:83]
	v_lshlrev_b32_e32 v82, 16, v139
	v_and_b32_e32 v83, 0xffff0000, v139
	v_pk_add_f32 v[2:3], v[2:3], v[82:83]
	v_lshlrev_b32_e32 v82, 16, v138
	v_and_b32_e32 v83, 0xffff0000, v138
	v_pk_add_f32 v[4:5], v[4:5], v[82:83]
	v_lshlrev_b32_e32 v82, 16, v140
	v_and_b32_e32 v83, 0xffff0000, v140
	v_pk_add_f32 v[4:5], v[4:5], v[82:83]
	v_lshlrev_b32_e32 v82, 16, v141
	v_and_b32_e32 v83, 0xffff0000, v141
	v_pk_add_f32 v[2:3], v[2:3], v[82:83]
	v_lshlrev_b32_e32 v82, 16, v143
	v_and_b32_e32 v83, 0xffff0000, v143
	v_pk_add_f32 v[2:3], v[2:3], v[82:83]
	v_lshlrev_b32_e32 v82, 16, v142
	v_and_b32_e32 v83, 0xffff0000, v142
	v_pk_add_f32 v[4:5], v[4:5], v[82:83]
	v_lshlrev_b32_e32 v82, 16, v144
	v_and_b32_e32 v83, 0xffff0000, v144
	v_pk_add_f32 v[4:5], v[4:5], v[82:83]
	v_lshlrev_b32_e32 v82, 16, v145
	v_and_b32_e32 v83, 0xffff0000, v145
	v_pk_add_f32 v[2:3], v[2:3], v[82:83]
	v_lshlrev_b32_e32 v82, 16, v147
	v_and_b32_e32 v83, 0xffff0000, v147
	v_pk_add_f32 v[2:3], v[2:3], v[82:83]
	v_lshlrev_b32_e32 v82, 16, v146
	v_and_b32_e32 v83, 0xffff0000, v146
	v_pk_add_f32 v[4:5], v[4:5], v[82:83]
	v_lshlrev_b32_e32 v82, 16, v148
	v_and_b32_e32 v83, 0xffff0000, v148
	v_pk_add_f32 v[4:5], v[4:5], v[82:83]
	v_lshlrev_b32_e32 v82, 16, v149
	v_and_b32_e32 v83, 0xffff0000, v149
	v_pk_add_f32 v[2:3], v[2:3], v[82:83]
	v_lshlrev_b32_e32 v82, 16, v151
	v_and_b32_e32 v83, 0xffff0000, v151
	v_pk_add_f32 v[2:3], v[2:3], v[82:83]
	v_lshlrev_b32_e32 v82, 16, v150
	v_and_b32_e32 v83, 0xffff0000, v150
	v_pk_add_f32 v[4:5], v[4:5], v[82:83]
	v_lshlrev_b32_e32 v82, 16, v152
	v_and_b32_e32 v83, 0xffff0000, v152
	v_pk_add_f32 v[4:5], v[4:5], v[82:83]
	v_lshlrev_b32_e32 v82, 16, v153
	v_and_b32_e32 v83, 0xffff0000, v153
	v_pk_add_f32 v[2:3], v[2:3], v[82:83]
	v_lshlrev_b32_e32 v82, 16, v155
	v_and_b32_e32 v83, 0xffff0000, v155
	v_pk_add_f32 v[2:3], v[2:3], v[82:83]
	v_lshlrev_b32_e32 v82, 16, v154
	v_and_b32_e32 v83, 0xffff0000, v154
	v_pk_add_f32 v[4:5], v[4:5], v[82:83]
	v_lshlrev_b32_e32 v82, 16, v156
	v_and_b32_e32 v83, 0xffff0000, v156
	v_pk_add_f32 v[4:5], v[4:5], v[82:83]
	v_lshlrev_b32_e32 v82, 16, v157
	v_and_b32_e32 v83, 0xffff0000, v157
	v_pk_add_f32 v[2:3], v[2:3], v[82:83]
	v_lshlrev_b32_e32 v82, 16, v159
	v_and_b32_e32 v83, 0xffff0000, v159
	v_pk_add_f32 v[2:3], v[2:3], v[82:83]
	v_lshlrev_b32_e32 v82, 16, v158
	v_and_b32_e32 v83, 0xffff0000, v158
	v_pk_add_f32 v[4:5], v[4:5], v[82:83]
	v_lshlrev_b32_e32 v82, 16, v160
	v_and_b32_e32 v83, 0xffff0000, v160
	v_pk_add_f32 v[4:5], v[4:5], v[82:83]
	v_lshlrev_b32_e32 v82, 16, v161
	v_and_b32_e32 v83, 0xffff0000, v161
	v_pk_add_f32 v[2:3], v[2:3], v[82:83]
	v_lshlrev_b32_e32 v82, 16, v163
	v_and_b32_e32 v83, 0xffff0000, v163
	v_pk_add_f32 v[2:3], v[2:3], v[82:83]
	v_lshlrev_b32_e32 v82, 16, v162
	v_and_b32_e32 v83, 0xffff0000, v162
	v_pk_add_f32 v[4:5], v[4:5], v[82:83]
	v_lshlrev_b32_e32 v82, 16, v164
	v_and_b32_e32 v83, 0xffff0000, v164
	v_pk_add_f32 v[4:5], v[4:5], v[82:83]
	v_lshlrev_b32_e32 v82, 16, v165
	v_and_b32_e32 v83, 0xffff0000, v165
	v_pk_add_f32 v[2:3], v[2:3], v[82:83]
	v_lshlrev_b32_e32 v82, 16, v167
	v_and_b32_e32 v83, 0xffff0000, v167
	v_pk_add_f32 v[2:3], v[2:3], v[82:83]
	v_lshlrev_b32_e32 v82, 16, v166
	v_and_b32_e32 v83, 0xffff0000, v166
	v_pk_add_f32 v[4:5], v[4:5], v[82:83]
	v_lshlrev_b32_e32 v82, 16, v168
	v_and_b32_e32 v83, 0xffff0000, v168
	v_pk_add_f32 v[4:5], v[4:5], v[82:83]
	v_lshlrev_b32_e32 v82, 16, v169
	v_and_b32_e32 v83, 0xffff0000, v169
	v_pk_add_f32 v[2:3], v[2:3], v[82:83]
	v_lshlrev_b32_e32 v82, 16, v171
	v_and_b32_e32 v83, 0xffff0000, v171
	v_pk_add_f32 v[2:3], v[2:3], v[82:83]
	v_lshlrev_b32_e32 v82, 16, v170
	v_and_b32_e32 v83, 0xffff0000, v170
	v_pk_add_f32 v[4:5], v[4:5], v[82:83]
	v_lshlrev_b32_e32 v82, 16, v172
	v_and_b32_e32 v83, 0xffff0000, v172
	v_pk_add_f32 v[4:5], v[4:5], v[82:83]
	v_lshlrev_b32_e32 v82, 16, v173
	v_and_b32_e32 v83, 0xffff0000, v173
	v_pk_add_f32 v[2:3], v[2:3], v[82:83]
	v_lshlrev_b32_e32 v82, 16, v175
	v_and_b32_e32 v83, 0xffff0000, v175
	v_pk_add_f32 v[2:3], v[2:3], v[82:83]
	v_lshlrev_b32_e32 v82, 16, v174
	v_and_b32_e32 v83, 0xffff0000, v174
	v_pk_add_f32 v[4:5], v[4:5], v[82:83]
	v_lshlrev_b32_e32 v82, 16, v176
	v_and_b32_e32 v83, 0xffff0000, v176
	v_pk_add_f32 v[4:5], v[4:5], v[82:83]
	v_lshlrev_b32_e32 v82, 16, v177
	v_and_b32_e32 v83, 0xffff0000, v177
	v_pk_add_f32 v[2:3], v[2:3], v[82:83]
	v_lshlrev_b32_e32 v82, 16, v179
	v_and_b32_e32 v83, 0xffff0000, v179
	v_pk_add_f32 v[2:3], v[2:3], v[82:83]
	v_lshlrev_b32_e32 v82, 16, v178
	v_and_b32_e32 v83, 0xffff0000, v178
	v_pk_add_f32 v[4:5], v[4:5], v[82:83]
	v_lshlrev_b32_e32 v82, 16, v180
	v_and_b32_e32 v83, 0xffff0000, v180
	v_pk_add_f32 v[4:5], v[4:5], v[82:83]
	v_lshlrev_b32_e32 v82, 16, v181
	v_and_b32_e32 v83, 0xffff0000, v181
	v_pk_add_f32 v[2:3], v[2:3], v[82:83]
	v_lshlrev_b32_e32 v82, 16, v183
	v_and_b32_e32 v83, 0xffff0000, v183
	v_pk_add_f32 v[2:3], v[2:3], v[82:83]
	v_lshlrev_b32_e32 v82, 16, v182
	v_and_b32_e32 v83, 0xffff0000, v182
	v_pk_add_f32 v[4:5], v[4:5], v[82:83]
	v_lshlrev_b32_e32 v82, 16, v184
	v_and_b32_e32 v83, 0xffff0000, v184
	v_pk_add_f32 v[4:5], v[4:5], v[82:83]
	v_lshlrev_b32_e32 v82, 16, v185
	v_and_b32_e32 v83, 0xffff0000, v185
	v_pk_add_f32 v[2:3], v[2:3], v[82:83]
	v_lshlrev_b32_e32 v82, 16, v187
	v_and_b32_e32 v83, 0xffff0000, v187
	v_pk_add_f32 v[2:3], v[2:3], v[82:83]
	v_lshlrev_b32_e32 v82, 16, v186
	v_and_b32_e32 v83, 0xffff0000, v186
	v_pk_add_f32 v[4:5], v[4:5], v[82:83]
	v_lshlrev_b32_e32 v82, 16, v188
	v_and_b32_e32 v83, 0xffff0000, v188
	v_pk_add_f32 v[4:5], v[4:5], v[82:83]
	v_lshlrev_b32_e32 v82, 16, v189
	v_and_b32_e32 v83, 0xffff0000, v189
	v_pk_add_f32 v[2:3], v[2:3], v[82:83]
	v_lshlrev_b32_e32 v82, 16, v191
	v_and_b32_e32 v83, 0xffff0000, v191
	v_pk_add_f32 v[2:3], v[2:3], v[82:83]
	v_lshlrev_b32_e32 v82, 16, v190
	v_and_b32_e32 v83, 0xffff0000, v190
	v_pk_add_f32 v[4:5], v[4:5], v[82:83]
	v_lshlrev_b32_e32 v82, 16, v192
	v_and_b32_e32 v83, 0xffff0000, v192
	v_pk_add_f32 v[4:5], v[4:5], v[82:83]
	v_lshlrev_b32_e32 v82, 16, v193
	v_and_b32_e32 v83, 0xffff0000, v193
	v_pk_add_f32 v[2:3], v[2:3], v[82:83]
	v_lshlrev_b32_e32 v82, 16, v195
	v_and_b32_e32 v83, 0xffff0000, v195
	v_pk_add_f32 v[2:3], v[2:3], v[82:83]
	v_lshlrev_b32_e32 v82, 16, v194
	v_and_b32_e32 v83, 0xffff0000, v194
	v_pk_add_f32 v[4:5], v[4:5], v[82:83]
	v_lshlrev_b32_e32 v82, 16, v196
	v_and_b32_e32 v83, 0xffff0000, v196
	v_pk_add_f32 v[4:5], v[4:5], v[82:83]
	v_lshlrev_b32_e32 v82, 16, v197
	v_and_b32_e32 v83, 0xffff0000, v197
	v_pk_add_f32 v[2:3], v[2:3], v[82:83]
	v_lshlrev_b32_e32 v82, 16, v199
	v_and_b32_e32 v83, 0xffff0000, v199
	v_pk_add_f32 v[2:3], v[2:3], v[82:83]
	v_lshlrev_b32_e32 v82, 16, v198
	v_and_b32_e32 v83, 0xffff0000, v198
	v_pk_add_f32 v[4:5], v[4:5], v[82:83]
	v_lshlrev_b32_e32 v82, 16, v200
	v_and_b32_e32 v83, 0xffff0000, v200
	v_pk_add_f32 v[4:5], v[4:5], v[82:83]
	v_lshlrev_b32_e32 v82, 16, v201
	v_and_b32_e32 v83, 0xffff0000, v201
	v_pk_add_f32 v[2:3], v[2:3], v[82:83]
	v_lshlrev_b32_e32 v82, 16, v203
	v_and_b32_e32 v83, 0xffff0000, v203
	v_pk_add_f32 v[2:3], v[2:3], v[82:83]
	v_lshlrev_b32_e32 v82, 16, v202
	v_and_b32_e32 v83, 0xffff0000, v202
	v_pk_add_f32 v[4:5], v[4:5], v[82:83]
	v_lshlrev_b32_e32 v82, 16, v204
	v_and_b32_e32 v83, 0xffff0000, v204
	v_pk_add_f32 v[4:5], v[4:5], v[82:83]
	v_lshlrev_b32_e32 v82, 16, v205
	v_and_b32_e32 v83, 0xffff0000, v205
	v_pk_add_f32 v[2:3], v[2:3], v[82:83]
	v_lshlrev_b32_e32 v82, 16, v207
	v_and_b32_e32 v83, 0xffff0000, v207
	v_pk_add_f32 v[2:3], v[2:3], v[82:83]
	v_lshlrev_b32_e32 v82, 16, v206
	v_and_b32_e32 v83, 0xffff0000, v206
	v_pk_add_f32 v[4:5], v[4:5], v[82:83]
	v_lshlrev_b32_e32 v82, 16, v208
	v_and_b32_e32 v83, 0xffff0000, v208
	v_pk_add_f32 v[4:5], v[4:5], v[82:83]
	v_lshlrev_b32_e32 v82, 16, v209
	v_and_b32_e32 v83, 0xffff0000, v209
	v_pk_add_f32 v[2:3], v[2:3], v[82:83]
	v_lshlrev_b32_e32 v82, 16, v211
	v_and_b32_e32 v83, 0xffff0000, v211
	v_pk_add_f32 v[2:3], v[2:3], v[82:83]
	v_lshlrev_b32_e32 v82, 16, v210
	v_and_b32_e32 v83, 0xffff0000, v210
	v_pk_add_f32 v[4:5], v[4:5], v[82:83]
	v_lshlrev_b32_e32 v82, 16, v212
	v_and_b32_e32 v83, 0xffff0000, v212
	v_pk_add_f32 v[4:5], v[4:5], v[82:83]
	v_lshlrev_b32_e32 v82, 16, v213
	v_and_b32_e32 v83, 0xffff0000, v213
	v_pk_add_f32 v[2:3], v[2:3], v[82:83]
	v_lshlrev_b32_e32 v82, 16, v215
	v_and_b32_e32 v83, 0xffff0000, v215
	v_pk_add_f32 v[2:3], v[2:3], v[82:83]
	v_lshlrev_b32_e32 v82, 16, v214
	v_and_b32_e32 v83, 0xffff0000, v214
	v_pk_add_f32 v[4:5], v[4:5], v[82:83]
	v_lshlrev_b32_e32 v82, 16, v216
	v_and_b32_e32 v83, 0xffff0000, v216
	v_pk_add_f32 v[4:5], v[4:5], v[82:83]
	v_lshlrev_b32_e32 v82, 16, v217
	v_and_b32_e32 v83, 0xffff0000, v217
	v_pk_add_f32 v[2:3], v[2:3], v[82:83]
	v_lshlrev_b32_e32 v82, 16, v219
	v_and_b32_e32 v83, 0xffff0000, v219
	v_pk_add_f32 v[2:3], v[2:3], v[82:83]
	v_lshlrev_b32_e32 v82, 16, v218
	v_and_b32_e32 v83, 0xffff0000, v218
	v_pk_add_f32 v[4:5], v[4:5], v[82:83]
	v_lshlrev_b32_e32 v82, 16, v220
	v_and_b32_e32 v83, 0xffff0000, v220
	v_pk_add_f32 v[4:5], v[4:5], v[82:83]
	v_lshlrev_b32_e32 v82, 16, v221
	v_and_b32_e32 v83, 0xffff0000, v221
	v_pk_add_f32 v[2:3], v[2:3], v[82:83]
	v_lshlrev_b32_e32 v82, 16, v223
	v_and_b32_e32 v83, 0xffff0000, v223
	v_pk_add_f32 v[2:3], v[2:3], v[82:83]
	v_lshlrev_b32_e32 v82, 16, v222
	v_and_b32_e32 v83, 0xffff0000, v222
	v_pk_add_f32 v[4:5], v[4:5], v[82:83]
	v_lshlrev_b32_e32 v82, 16, v6
	v_and_b32_e32 v83, 0xffff0000, v6
	v_pk_add_f32 v[4:5], v[4:5], v[82:83]
	v_lshlrev_b32_e32 v82, 16, v7
	v_and_b32_e32 v83, 0xffff0000, v7
	v_pk_add_f32 v[2:3], v[2:3], v[82:83]
	v_lshlrev_b32_e32 v82, 16, v9
	v_and_b32_e32 v83, 0xffff0000, v9
	v_pk_add_f32 v[2:3], v[2:3], v[82:83]
	v_lshlrev_b32_e32 v82, 16, v8
	v_and_b32_e32 v83, 0xffff0000, v8
	v_pk_add_f32 v[4:5], v[4:5], v[82:83]
	v_lshlrev_b32_e32 v82, 16, v10
	v_and_b32_e32 v83, 0xffff0000, v10
	v_pk_add_f32 v[4:5], v[4:5], v[82:83]
	v_lshlrev_b32_e32 v82, 16, v11
	v_and_b32_e32 v83, 0xffff0000, v11
	v_pk_add_f32 v[2:3], v[2:3], v[82:83]
	v_lshlrev_b32_e32 v82, 16, v13
	v_and_b32_e32 v83, 0xffff0000, v13
	v_pk_add_f32 v[2:3], v[2:3], v[82:83]
	v_lshlrev_b32_e32 v82, 16, v12
	v_and_b32_e32 v83, 0xffff0000, v12
	v_pk_add_f32 v[4:5], v[4:5], v[82:83]
	v_lshlrev_b32_e32 v82, 16, v14
	v_and_b32_e32 v83, 0xffff0000, v14
	v_pk_add_f32 v[4:5], v[4:5], v[82:83]
	v_lshlrev_b32_e32 v82, 16, v15
	v_and_b32_e32 v83, 0xffff0000, v15
	v_pk_add_f32 v[2:3], v[2:3], v[82:83]
	v_lshlrev_b32_e32 v82, 16, v17
	v_and_b32_e32 v83, 0xffff0000, v17
	v_pk_add_f32 v[2:3], v[2:3], v[82:83]
	v_lshlrev_b32_e32 v82, 16, v16
	v_and_b32_e32 v83, 0xffff0000, v16
	v_pk_add_f32 v[4:5], v[4:5], v[82:83]
	v_lshlrev_b32_e32 v82, 16, v18
	v_and_b32_e32 v83, 0xffff0000, v18
	v_pk_add_f32 v[4:5], v[4:5], v[82:83]
	v_lshlrev_b32_e32 v82, 16, v19
	v_and_b32_e32 v83, 0xffff0000, v19
	v_pk_add_f32 v[2:3], v[2:3], v[82:83]
	v_lshlrev_b32_e32 v82, 16, v21
	v_and_b32_e32 v83, 0xffff0000, v21
	v_pk_add_f32 v[2:3], v[2:3], v[82:83]
	v_lshlrev_b32_e32 v82, 16, v20
	v_and_b32_e32 v83, 0xffff0000, v20
	v_pk_add_f32 v[4:5], v[4:5], v[82:83]
	v_mbcnt_lo_u32_b32 v0, -1, 0
	v_mbcnt_hi_u32_b32 v0, -1, v0
	v_mbcnt_lo_u32_b32 v6, -1, 0
	v_mbcnt_hi_u32_b32 v6, -1, v6
	v_mbcnt_lo_u32_b32 v1, -1, 0
	v_mbcnt_hi_u32_b32 v1, -1, v1
	s_nop 0
	v_lshlrev_b32_e32 v0, 2, v0
	v_lshlrev_b32_e32 v1, 2, v1
	v_xor_b32_e32 v0, 64, v0
	v_xor_b32_e32 v1, 64, v1
	ds_bpermute_b32 v0, v0, v4
	ds_bpermute_b32 v1, v1, v5
	v_lshlrev_b32_e32 v6, 2, v6
	v_xor_b32_e32 v6, 0x80, v6
	s_waitcnt lgkmcnt(0)
	v_pk_add_f32 v[0:1], v[4:5], v[0:1]
	ds_bpermute_b32 v4, v6, v0
	v_mbcnt_lo_u32_b32 v5, -1, 0
	v_mbcnt_hi_u32_b32 v5, -1, v5
	v_mbcnt_lo_u32_b32 v6, -1, 0
	v_mbcnt_hi_u32_b32 v6, -1, v6
	v_mbcnt_lo_u32_b32 v8, -1, 0
	v_mbcnt_hi_u32_b32 v8, -1, v8
	v_mbcnt_lo_u32_b32 v7, -1, 0
	v_mbcnt_hi_u32_b32 v7, -1, v7
	s_nop 0
	v_lshlrev_b32_e32 v6, 2, v6
	v_lshlrev_b32_e32 v7, 2, v7
	v_xor_b32_e32 v6, 64, v6
	v_xor_b32_e32 v7, 64, v7
	ds_bpermute_b32 v6, v6, v2
	ds_bpermute_b32 v7, v7, v3
	v_lshlrev_b32_e32 v5, 2, v5
	v_lshlrev_b32_e32 v8, 2, v8
	v_xor_b32_e32 v5, 0x80, v5
	v_xor_b32_e32 v8, 0x80, v8
	s_waitcnt lgkmcnt(0)
	v_pk_add_f32 v[2:3], v[2:3], v[6:7]
	v_mbcnt_lo_u32_b32 v7, -1, 0
	v_mbcnt_hi_u32_b32 v7, -1, v7
	ds_bpermute_b32 v5, v5, v1
	v_lshlrev_b32_e32 v7, 2, v7
	v_xor_b32_e32 v7, 0x80, v7
	ds_bpermute_b32 v6, v8, v2
	ds_bpermute_b32 v7, v7, v3
	s_and_saveexec_b64 s[14:15], s[36:37]
	s_cbranch_execz .LBB0_354
	s_and_b32 s19, s18, 0x7fffffff
	s_add_i32 s30, s19, 0xfffff400
	s_mov_b32 s31, s87
	s_lshl_b64 s[30:31], s[30:31], 8
	s_waitcnt lgkmcnt(2)
	v_pk_add_f32 v[0:1], v[0:1], v[4:5]
	s_waitcnt lgkmcnt(0)
	v_pk_add_f32 v[2:3], v[2:3], v[6:7]
	v_lshl_add_u64 v[4:5], v[32:33], 0, s[30:31]
	s_mov_b32 s30, 0x3b800000
	v_pk_mul_f32 v[2:3], v[2:3], s[30:31] op_sel_hi:[1,0]
	v_pk_mul_f32 v[0:1], v[0:1], s[30:31] op_sel_hi:[1,0]
	global_store_dwordx4 v[4:5], v[0:3], off

.LBB0_355:
	s_and_b64 vcc, exec, s[14:15]
	s_cbranch_vccz .LBB0_359
	s_add_i32 s14, s18, 0xfffffc00
	s_lshr_b32 s19, s14, 3
	s_lshl_b32 s14, s18, 21
	s_and_b32 s14, s14, 0x800000
	v_readlane_b32 s15, v254, 39
	s_add_u32 s14, s15, s14
	v_readlane_b32 s15, v254, 41
	v_lshl_or_b32 v96, s19, 6, v35
	s_addc_u32 s15, s15, 0
	s_waitcnt lgkmcnt(0)
	v_lshlrev_b64 v[0:1], 9, v[96:97]
	v_lshl_add_u64 v[0:1], s[14:15], 0, v[0:1]
	s_lshl_b32 s14, s18, 7
	s_and_b32 s14, s14, 0x180
	s_mov_b32 s15, s87
	v_lshl_add_u64 v[12:13], v[0:1], 0, s[14:15]
	global_load_dwordx4 v[0:3], v[12:13], off offset:48
	s_waitcnt lgkmcnt(0)
	global_load_dwordx4 v[4:7], v[12:13], off offset:32
	global_load_dwordx4 v[8:11], v[12:13], off offset:16
	global_load_dwordx4 v[14:17], v[12:13], off
	global_load_dwordx4 v[112:115], v[12:13], off offset:112
	global_load_dwordx4 v[116:119], v[12:13], off offset:96
	global_load_dwordx4 v[120:123], v[12:13], off offset:80
	global_load_dwordx4 v[124:127], v[12:13], off offset:64
	s_waitcnt vmcnt(4)
	v_lshlrev_b32_e32 v18, 16, v14
	v_and_b32_e32 v14, 0xffff0000, v14
	v_lshlrev_b32_e32 v19, 16, v15
	v_and_b32_e32 v15, 0xffff0000, v15
	v_mul_f32_e32 v14, v14, v14
	v_mul_f32_e32 v15, v15, v15
	v_lshlrev_b32_e32 v20, 16, v16
	v_and_b32_e32 v16, 0xffff0000, v16
	v_fmac_f32_e32 v14, v18, v18
	v_fmac_f32_e32 v15, v19, v19
	v_add_f32_e32 v14, v14, v15
	v_mul_f32_e32 v15, v16, v16
	v_lshlrev_b32_e32 v21, 16, v17
	v_and_b32_e32 v17, 0xffff0000, v17
	v_fmac_f32_e32 v15, v20, v20
	v_add_f32_e32 v14, v15, v14
	v_mul_f32_e32 v15, v17, v17
	v_fmac_f32_e32 v15, v21, v21
	v_add_f32_e32 v14, v15, v14
	v_lshlrev_b32_e32 v15, 16, v8
	v_and_b32_e32 v8, 0xffff0000, v8
	v_lshlrev_b32_e32 v16, 16, v9
	v_and_b32_e32 v9, 0xffff0000, v9
	v_mul_f32_e32 v8, v8, v8
	v_mul_f32_e32 v9, v9, v9
	v_lshlrev_b32_e32 v17, 16, v10
	v_and_b32_e32 v10, 0xffff0000, v10
	v_fmac_f32_e32 v8, v15, v15
	v_fmac_f32_e32 v9, v16, v16
	v_add_f32_e32 v8, v8, v9
	v_mul_f32_e32 v9, v10, v10
	v_lshlrev_b32_e32 v18, 16, v11
	v_and_b32_e32 v11, 0xffff0000, v11
	v_fmac_f32_e32 v9, v17, v17
	v_add_f32_e32 v8, v9, v8
	v_mul_f32_e32 v9, v11, v11
	v_fmac_f32_e32 v9, v18, v18
	v_add_f32_e32 v8, v9, v8
	v_lshlrev_b32_e32 v9, 16, v4
	v_and_b32_e32 v4, 0xffff0000, v4
	v_lshlrev_b32_e32 v10, 16, v5
	v_and_b32_e32 v5, 0xffff0000, v5
	v_mul_f32_e32 v4, v4, v4
	v_mul_f32_e32 v5, v5, v5
	v_lshlrev_b32_e32 v11, 16, v6
	v_and_b32_e32 v6, 0xffff0000, v6
	v_fmac_f32_e32 v4, v9, v9
	v_fmac_f32_e32 v5, v10, v10
	v_add_f32_e32 v4, v4, v5
	v_mul_f32_e32 v5, v6, v6
	v_add_f32_e32 v8, v14, v8
	v_lshlrev_b32_e32 v14, 16, v7
	v_and_b32_e32 v7, 0xffff0000, v7
	v_fmac_f32_e32 v5, v11, v11
	v_add_f32_e32 v4, v5, v4
	v_mul_f32_e32 v5, v7, v7
	v_fmac_f32_e32 v5, v14, v14
	v_add_f32_e32 v4, v5, v4
	v_lshlrev_b32_e32 v5, 16, v0
	v_and_b32_e32 v0, 0xffff0000, v0
	v_lshlrev_b32_e32 v6, 16, v1
	v_and_b32_e32 v1, 0xffff0000, v1
	v_mul_f32_e32 v0, v0, v0
	v_mul_f32_e32 v1, v1, v1
	v_lshlrev_b32_e32 v7, 16, v2
	v_and_b32_e32 v2, 0xffff0000, v2
	v_fmac_f32_e32 v0, v5, v5
	v_fmac_f32_e32 v1, v6, v6
	v_add_f32_e32 v0, v0, v1
	v_mul_f32_e32 v1, v2, v2
	v_add_f32_e32 v4, v8, v4
	v_lshlrev_b32_e32 v8, 16, v3
	v_and_b32_e32 v3, 0xffff0000, v3
	v_fmac_f32_e32 v1, v7, v7
	v_add_f32_e32 v0, v1, v0
	v_mul_f32_e32 v1, v3, v3
	v_fmac_f32_e32 v1, v8, v8
	v_add_f32_e32 v0, v1, v0
	v_add_f32_e32 v16, v4, v0
	s_waitcnt vmcnt(0)
	v_mov_b32_e32 v0, v112
	v_mov_b32_e32 v1, v113
	v_mov_b32_e32 v2, v114
	v_mov_b32_e32 v3, v115
	v_mov_b32_e32 v4, v116
	v_mov_b32_e32 v5, v117
	v_mov_b32_e32 v6, v118
	v_mov_b32_e32 v7, v119
	v_mov_b32_e32 v8, v120
	v_mov_b32_e32 v9, v121
	v_mov_b32_e32 v10, v122
	v_mov_b32_e32 v11, v123
	v_mov_b32_e32 v12, v124
	v_mov_b32_e32 v13, v125
	v_mov_b32_e32 v14, v126
	v_mov_b32_e32 v15, v127
	v_lshlrev_b32_e32 v17, 16, v12
	v_and_b32_e32 v12, 0xffff0000, v12
	v_lshlrev_b32_e32 v18, 16, v13
	v_and_b32_e32 v13, 0xffff0000, v13
	v_mul_f32_e32 v12, v12, v12
	v_mul_f32_e32 v13, v13, v13
	v_lshlrev_b32_e32 v19, 16, v14
	v_and_b32_e32 v14, 0xffff0000, v14
	v_fmac_f32_e32 v12, v17, v17
	v_fmac_f32_e32 v13, v18, v18
	v_add_f32_e32 v12, v12, v13
	v_mul_f32_e32 v13, v14, v14
	v_lshlrev_b32_e32 v20, 16, v15
	v_and_b32_e32 v15, 0xffff0000, v15
	v_fmac_f32_e32 v13, v19, v19
	v_add_f32_e32 v12, v13, v12
	v_mul_f32_e32 v13, v15, v15
	v_fmac_f32_e32 v13, v20, v20
	v_add_f32_e32 v12, v13, v12
	v_lshlrev_b32_e32 v13, 16, v8
	v_and_b32_e32 v8, 0xffff0000, v8
	v_lshlrev_b32_e32 v14, 16, v9
	v_and_b32_e32 v9, 0xffff0000, v9
	v_mul_f32_e32 v8, v8, v8
	v_mul_f32_e32 v9, v9, v9
	v_lshlrev_b32_e32 v15, 16, v10
	v_and_b32_e32 v10, 0xffff0000, v10
	v_fmac_f32_e32 v8, v13, v13
	v_fmac_f32_e32 v9, v14, v14
	v_add_f32_e32 v8, v8, v9
	v_mul_f32_e32 v9, v10, v10
	v_add_f32_e32 v12, v16, v12
	v_lshlrev_b32_e32 v16, 16, v11
	v_and_b32_e32 v11, 0xffff0000, v11
	v_fmac_f32_e32 v9, v15, v15
	v_add_f32_e32 v8, v9, v8
	v_mul_f32_e32 v9, v11, v11
	v_fmac_f32_e32 v9, v16, v16
	v_add_f32_e32 v8, v9, v8
	v_lshlrev_b32_e32 v9, 16, v4
	v_and_b32_e32 v4, 0xffff0000, v4
	v_lshlrev_b32_e32 v10, 16, v5
	v_and_b32_e32 v5, 0xffff0000, v5
	v_mul_f32_e32 v4, v4, v4
	v_mul_f32_e32 v5, v5, v5
	v_lshlrev_b32_e32 v11, 16, v6
	v_and_b32_e32 v6, 0xffff0000, v6
	v_fmac_f32_e32 v4, v9, v9
	v_fmac_f32_e32 v5, v10, v10
	v_add_f32_e32 v4, v4, v5
	v_mul_f32_e32 v5, v6, v6
	v_add_f32_e32 v8, v12, v8
	v_lshlrev_b32_e32 v12, 16, v7
	v_and_b32_e32 v7, 0xffff0000, v7
	v_fmac_f32_e32 v5, v11, v11
	v_add_f32_e32 v4, v5, v4
	v_mul_f32_e32 v5, v7, v7
	v_fmac_f32_e32 v5, v12, v12
	v_add_f32_e32 v4, v5, v4
	v_lshlrev_b32_e32 v5, 16, v0
	v_and_b32_e32 v0, 0xffff0000, v0
	v_lshlrev_b32_e32 v6, 16, v1
	v_and_b32_e32 v1, 0xffff0000, v1
	v_mul_f32_e32 v0, v0, v0
	v_mul_f32_e32 v1, v1, v1
	v_lshlrev_b32_e32 v7, 16, v2
	v_and_b32_e32 v2, 0xffff0000, v2
	v_fmac_f32_e32 v0, v5, v5
	v_fmac_f32_e32 v1, v6, v6
	v_add_f32_e32 v0, v0, v1
	v_mul_f32_e32 v1, v2, v2
	v_add_f32_e32 v4, v8, v4
	v_lshlrev_b32_e32 v8, 16, v3
	v_and_b32_e32 v3, 0xffff0000, v3
	v_fmac_f32_e32 v1, v7, v7
	v_add_f32_e32 v0, v1, v0
	v_mul_f32_e32 v1, v3, v3
	v_fmac_f32_e32 v1, v8, v8
	v_add_f32_e32 v0, v1, v0
	v_add_f32_e32 v0, v4, v0
	v_cmp_gt_f32_e32 vcc, s1, v0
	v_mul_f32_e32 v1, 0x4f800000, v0
	s_nop 0
	v_cndmask_b32_e32 v0, v0, v1, vcc
	v_sqrt_f32_e32 v1, v0
	s_nop 0
	v_add_u32_e32 v2, -1, v1
	v_fma_f32 v3, -v2, v1, v0
	v_cmp_ge_f32_e64 s[14:15], 0, v3
	v_add_u32_e32 v3, 1, v1
	s_nop 0
	v_cndmask_b32_e64 v2, v1, v2, s[14:15]
	v_fma_f32 v1, -v3, v1, v0
	v_cmp_lt_f32_e64 s[14:15], 0, v1
	s_nop 1
	v_cndmask_b32_e64 v1, v2, v3, s[14:15]
	v_mul_f32_e32 v2, 0x37800000, v1
	v_cndmask_b32_e32 v1, v1, v2, vcc
	v_cmp_class_f32_e32 vcc, v0, v240
	s_nop 1
	v_cndmask_b32_e32 v0, v1, v0, vcc
	v_mbcnt_lo_u32_b32 v1, -1, 0
	v_mbcnt_hi_u32_b32 v1, -1, v1
	s_nop 0
	v_lshlrev_b32_e32 v1, 2, v1
	v_xor_b32_e32 v1, 4, v1
	ds_bpermute_b32 v1, v1, v0
	s_waitcnt lgkmcnt(0)
	v_max_f32_e32 v1, v1, v1
	v_max_f32_e32 v0, v0, v1
	v_mbcnt_lo_u32_b32 v1, -1, 0
	v_mbcnt_hi_u32_b32 v1, -1, v1
	s_nop 0
	v_lshlrev_b32_e32 v1, 2, v1
	v_xor_b32_e32 v1, 8, v1
	ds_bpermute_b32 v1, v1, v0
	s_waitcnt lgkmcnt(0)
	v_max_f32_e32 v1, v1, v1
	v_max_f32_e32 v0, v0, v1
	v_mbcnt_lo_u32_b32 v1, -1, 0
	v_mbcnt_hi_u32_b32 v1, -1, v1
	s_nop 0
	v_lshlrev_b32_e32 v1, 2, v1
	v_xor_b32_e32 v1, 16, v1
	ds_bpermute_b32 v1, v1, v0
	s_waitcnt lgkmcnt(0)
	v_max_f32_e32 v1, v1, v1
	v_max_f32_e32 v0, v0, v1
	v_mbcnt_lo_u32_b32 v1, -1, 0
	v_mbcnt_hi_u32_b32 v1, -1, v1
	s_nop 0
	v_lshlrev_b32_e32 v1, 2, v1
	v_xor_b32_e32 v1, 32, v1
	ds_bpermute_b32 v1, v1, v0
	s_waitcnt lgkmcnt(0)
	v_max_f32_e32 v1, v1, v1
	v_max_f32_e32 v0, v0, v1
	v_mbcnt_lo_u32_b32 v1, -1, 0
	v_mbcnt_hi_u32_b32 v1, -1, v1
	s_nop 0
	v_lshlrev_b32_e32 v1, 2, v1
	v_xor_b32_e32 v1, 64, v1
	ds_bpermute_b32 v1, v1, v0
	s_waitcnt lgkmcnt(0)
	v_max_f32_e32 v1, v1, v1
	v_max_f32_e32 v0, v0, v1
	v_mbcnt_lo_u32_b32 v1, -1, 0
	v_mbcnt_hi_u32_b32 v1, -1, v1
	s_nop 0
	v_lshlrev_b32_e32 v1, 2, v1
	v_xor_b32_e32 v1, 0x80, v1
	ds_bpermute_b32 v1, v1, v0
	s_and_saveexec_b64 s[14:15], s[38:39]
	s_cbranch_execz .LBB0_358
	s_lshl_b32 s30, s18, 8
	s_and_b32 s30, s30, 0x700
	s_add_i32 s30, s30, s19
	s_waitcnt lgkmcnt(0)
	v_max_f32_e32 v1, v1, v1
	v_max_f32_e32 v0, v0, v0
	s_lshl_b32 s19, s30, 2
	v_readlane_b32 s30, v254, 43
	v_max_f32_e32 v0, v0, v1
	v_mov_b32_e32 v1, s19
	v_readlane_b32 s31, v254, 44
	s_nop 4
	global_store_dword v1, v0, s[30:31]
